# v59 + straight-line no-rescale path in both attention softmax blocks (skip 4 taken branches when all lanes under threshold)
# baseline (speedup 1.0000x reference)
.LBB0_1042:
	v_max3_f32 v90, v50, v51, v52
	v_max3_f32 v91, v53, v54, v55
	v_max3_f32 v92, v56, v57, v58
	v_max3_f32 v93, v59, v60, v61
	v_max3_f32 v90, v90, v62, v63
	v_max3_f32 v91, v91, v64, v65
	v_max3_f32 v92, v92, v34, v35
	v_max3_f32 v93, v93, v36, v37
	v_max3_f32 v90, v90, v38, v39
	v_max3_f32 v91, v91, v40, v41
	v_max3_f32 v92, v92, v42, v43
	v_max3_f32 v93, v93, v44, v45
	v_max3_f32 v90, v90, v46, v47
	v_max3_f32 v91, v91, v48, v49
	v_max3_f32 v90, v90, v92, v93
	v_max_f32_e32 v90, v90, v91
	v_mov_b32_e32 v91, v90
	s_nop 1
	v_permlane32_swap_b32_e32 v90, v91
	s_cmp_eq_u32 s86, 1
	s_cselect_b64 s[12:13], -1, 0
	s_cmp_lg_u32 s86, 1
	v_max_f32_e32 v91, v90, v91
	s_cbranch_scc0 .LBB0_1060
	s_mov_b32 s14, 0x41000000
	v_cmp_ge_f32_e32 vcc, s14, v91
	s_cmp_lg_u64 vcc, exec
	s_mov_b64 s[16:17], 0
	s_mov_b64 s[14:15], 0
	s_cbranch_scc1 .Lmy_mla_upd
	v_mov_b32_e32 v91, 1.0
	s_branch .LBB0_1066
.Lmy_mla_upd:
	v_max_f32_e32 v90, 0, v91
	s_mov_b64 s[14:15], -1
	s_and_b64 vcc, exec, s[16:17]
	s_cbranch_vccz .LBB0_1061
	s_branch .LBB0_1058

.LBB0_1056:
	s_waitcnt vmcnt(4) lgkmcnt(0)
	s_barrier
	s_cbranch_execz .LBB0_1052
	s_branch .LBB0_1053
.LBB0_1058:
	v_mov_b32_e32 v90, v91
	v_mov_b32_e32 v91, 1.0
	s_branch .LBB0_1062

.LBB0_1093:
	v_max3_f32 v0, v66, v67, v68
	v_max3_f32 v114, v69, v70, v71
	v_max3_f32 v115, v72, v73, v74
	v_max3_f32 v116, v75, v76, v77
	v_max3_f32 v0, v0, v78, v79
	v_max3_f32 v114, v114, v80, v81
	v_max3_f32 v115, v115, v82, v83
	v_max3_f32 v116, v116, v84, v85
	v_max3_f32 v0, v0, v86, v87
	v_max3_f32 v114, v114, v88, v89
	v_max3_f32 v115, v115, v90, v91
	v_max3_f32 v116, v116, v92, v93
	v_max3_f32 v0, v0, v94, v95
	v_max3_f32 v114, v114, v96, v97
	v_max3_f32 v0, v0, v115, v116
	v_max_f32_e32 v0, v0, v114
	v_mov_b32_e32 v114, v0
	s_nop 1
	v_permlane32_swap_b32_e32 v0, v114
	s_cmp_eq_u32 s78, 1
	s_cselect_b64 s[12:13], -1, 0
	s_cmp_lg_u32 s78, 1
	v_max_f32_e32 v114, v0, v114
	s_cbranch_scc0 .LBB0_1111
	s_mov_b32 s5, 0x41000000
	v_cmp_ge_f32_e32 vcc, s5, v114
	s_cmp_lg_u64 vcc, exec
	s_mov_b64 s[16:17], 0
	s_mov_b64 s[14:15], 0
	s_cbranch_scc1 .Lmy_diff_upd
	v_mov_b32_e32 v114, 1.0
	s_branch .LBB0_1117
.Lmy_diff_upd:
	v_max_f32_e32 v0, 0, v114
	s_mov_b64 s[14:15], -1
	s_and_b64 vcc, exec, s[16:17]
	s_cbranch_vccz .LBB0_1112
	s_branch .LBB0_1109

.LBB0_1107:
	s_waitcnt vmcnt(3) lgkmcnt(0)
	s_barrier
	s_cbranch_execz .LBB0_1103
	s_branch .LBB0_1104
.LBB0_1109:
	v_mov_b32_e32 v0, v114
	v_mov_b32_e32 v114, 1.0
	s_branch .LBB0_1113
